# g13: g11 + P6 gate-up bias folded into the accumulators (next unit's bias DMA'd one unit ahead, C operand of the first MFMAs; epilogue bias add removed)
# speedup vs baseline: 1.0076x; 1.0076x over previous
.LBB0_598:
	s_or_b64 exec, exec, s[0:1]
	v_cmp_lt_i32_e32 vcc, s2, v162
	v_readfirstlane_b32 s0, v0
	s_waitcnt lgkmcnt(0)
	s_barrier
	s_cbranch_vccz .LBB0_626
	v_lshlrev_b32_e32 v2, 4, v0
	v_and_b32_e32 v1, 32, v0
	v_bfe_u32 v4, v0, 2, 4
	v_bitop3_b32 v1, v2, v1, 48 bitop3:0x6c
	v_lshrrev_b32_e32 v5, 3, v0
	v_or_b32_e32 v2, 0x2000, v2
	s_add_u32 s46, s96, 0x4000000
	v_and_or_b32 v180, v5, 48, v4
	v_lshrrev_b32_e32 v5, 7, v2
	s_movk_i32 s6, 0x70
	s_addc_u32 s47, s97, 0
	s_lshr_b32 s5, s0, 6
	v_and_or_b32 v181, v5, s6, v4
	v_lshrrev_b32_e32 v5, 5, v0
	s_lshr_b32 s1, s0, 8
	v_and_b32_e32 v6, 48, v0
	s_lshl_b32 s48, s5, 10
	v_bfe_u32 v4, v0, 2, 2
	v_and_b32_e32 v5, 4, v5
	s_add_u32 s10, s96, 0x5e800000
	v_lshrrev_b32_e32 v2, 6, v2
	v_or3_b32 v4, v4, v5, v6
	s_movk_i32 s6, 0xc0
	s_addc_u32 s11, s97, 0
	v_and_or_b32 v2, v2, s6, v4
	s_lshr_b32 s6, s3, 29
	s_add_i32 s6, s2, s6
	s_lshl_b32 s49, s44, 1
	s_ashr_i32 s7, s6, 3
	s_and_b32 s6, s6, -8
	s_sub_i32 s6, s2, s6
	s_or_b32 s50, s49, 1
	s_cmp_lt_i32 s6, 0
	s_cselect_b32 s12, s50, s49
	s_mul_i32 s6, s12, s6
	s_add_i32 s6, s6, s7
	s_ashr_i32 s7, s6, 31
	s_lshr_b32 s7, s7, 26
	s_add_i32 s7, s6, s7
	s_ashr_i32 s12, s7, 6
	s_lshl_b32 s12, s12, 2
	s_sub_i32 s13, s44, s12
	s_min_i32 s13, s13, 4
	s_abs_i32 s14, s13
	v_cvt_f32_u32_e32 v5, s14
	v_lshrrev_b32_e32 v3, 2, v0
	v_and_or_b32 v1, v0, 64, v1
	v_lshl_or_b32 v164, v2, 11, v1
	v_and_or_b32 v2, v3, 64, v4
	v_lshl_or_b32 v166, v2, 11, v1
	v_rcp_iflag_f32_e32 v2, v5
	s_sub_i32 s16, 0, s14
	s_andn2_b32 s7, s7, 63
	s_sub_i32 s6, s6, s7
	v_mul_f32_e32 v2, 0x4f7ffffe, v2
	v_cvt_u32_f32_e32 v2, v2
	s_abs_i32 s15, s6
	s_xor_b32 s7, s6, s13
	s_ashr_i32 s7, s7, 31
	v_readfirstlane_b32 s17, v2
	s_mul_i32 s16, s16, s17
	s_mul_hi_u32 s16, s17, s16
	s_add_i32 s17, s17, s16
	s_mul_hi_u32 s16, s15, s17
	s_mul_i32 s17, s16, s14
	s_sub_i32 s15, s15, s17
	s_add_i32 s17, s16, 1
	s_sub_i32 s18, s15, s14
	s_cmp_ge_u32 s15, s14
	s_cselect_b32 s16, s17, s16
	s_cselect_b32 s15, s18, s15
	s_add_i32 s17, s16, 1
	s_cmp_ge_u32 s15, s14
	s_cselect_b32 s14, s17, s16
	s_xor_b32 s14, s14, s7
	s_sub_i32 s7, s14, s7
	s_mul_i32 s13, s7, s13
	s_sub_i32 s6, s6, s13
	s_add_i32 s64, s12, s6
	s_add_i32 s6, s64, 0
	v_lshlrev_b32_e32 v3, 1, v180
	v_lshlrev_b32_e32 v5, 1, v181
	s_add_i32 s6, s6, 0x23c40
	v_add_u32_e32 v4, s4, v3
	v_add_u32_e32 v7, s4, v5
	s_add_i32 s4, 0, 0x20100
	v_mov_b32_e32 v2, s6
	v_add_u32_e32 v3, s4, v3
	v_add_u32_e32 v5, s4, v5
	ds_read_u8 v2, v2
	ds_read_u16 v4, v4
	ds_read_u16 v7, v7
	ds_read_u16 v3, v3
	ds_read_u16 v5, v5
	s_waitcnt lgkmcnt(4)
	v_readfirstlane_b32 s4, v2
	s_lshl_b32 s4, s4, 4
	s_add_i32 s38, s4, s7
	s_ashr_i32 s39, s38, 31
	s_ashr_i32 s12, s38, 4
	s_ashr_i32 s13, s12, 31
	s_lshl_b64 s[12:13], s[12:13], 14
	v_readlane_b32 s14, v254, 4
	v_readlane_b32 s15, v254, 5
	s_lshl_b32 s16, s38, 10
	s_and_b32 s16, s16, 0x3c00
	s_nop 3
	s_add_u32 s12, s14, s12
	s_addc_u32 s13, s15, s13
	s_add_u32 s12, s12, s16
	s_addc_u32 s13, s13, 0
	v_lshlrev_b32_e32 v2, 4, v186
	s_add_i32 m0, 0, 0x22400
	s_nop 0
	global_load_lds_dwordx4 v2, s[12:13]
	s_lshl_b64 s[6:7], s[38:39], 19
	s_add_u32 s40, s46, s6
	s_addc_u32 s41, s47, s7
	s_add_i32 s39, s48, 0
	s_add_i32 m0, s39, 0x10000
	s_waitcnt lgkmcnt(3)
	v_lshl_or_b32 v168, v4, 11, v1
	global_load_lds_dwordx4 v166, s[40:41]
	s_add_i32 m0, s39, 0x12000
	s_add_u32 s6, s40, 0x4000
	global_load_lds_dwordx4 v164, s[40:41]
	s_addc_u32 s7, s41, 0
	s_add_i32 m0, s39, 0x14000
	s_add_i32 s51, s39, 0x2000
	global_load_lds_dwordx4 v166, s[6:7]
	s_add_i32 m0, s39, 0x16000
	s_waitcnt lgkmcnt(0)
	v_lshl_or_b32 v170, v7, 11, v1
	global_load_lds_dwordx4 v164, s[6:7]
	s_mov_b32 m0, s39
	s_add_i32 s52, s39, 0x4000
	global_load_lds_dwordx4 v168, s[10:11]
	s_mov_b32 m0, s51
	v_lshl_or_b32 v172, v3, 11, v1
	global_load_lds_dwordx4 v170, s[10:11]
	s_mov_b32 m0, s52
	s_add_i32 s53, s39, 0x6000
	v_lshl_or_b32 v174, v5, 11, v1
	global_load_lds_dwordx4 v172, s[10:11]
	s_mov_b32 m0, s53
	v_mov_b32_e32 v169, 0
	global_load_lds_dwordx4 v174, s[10:11]
	v_mov_b32_e32 v167, v169
	v_mov_b32_e32 v165, v169
	s_cmp_eq_u32 s1, 1
	s_mov_b32 s6, 0
	v_lshl_add_u64 v[4:5], s[40:41], 0, v[166:167]
	v_lshl_add_u64 v[2:3], s[40:41], 0, v[164:165]
	s_cselect_b64 s[12:13], -1, 0
	s_cmp_lg_u32 s1, 1
	v_mov_b32_e32 v171, v169
	s_cbranch_scc1 .LBB0_601
	s_barrier

.LBB0_608:
	s_and_b64 vcc, s[20:21], s[4:5]
	s_lshl_b32 s65, s6, 10
	s_cbranch_vccz .LBB0_610
	s_ashr_i32 s6, s34, 4
	v_readlane_b32 s68, v254, 2
	s_ashr_i32 s7, s6, 31
	v_readlane_b32 s70, v254, 4
	v_readlane_b32 s71, v254, 5
	s_lshl_b64 s[6:7], s[6:7], 14
	s_mov_b64 s[66:67], s[70:71]
	s_add_u32 s6, s66, s6
	s_addc_u32 s7, s67, s7
	s_lshl_b32 s35, s34, 10
	s_and_b32 s35, s35, 0x3c00
	s_add_u32 s6, s6, s35
	s_addc_u32 s7, s7, 0
	s_xor_b32 s35, s65, 0x400
	s_add_i32 m0, s35, 0x22400
	v_readlane_b32 s69, v254, 3
	global_load_lds_dwordx4 v187, s[6:7]
	v_readlane_b32 s72, v254, 6
	v_readlane_b32 s73, v254, 7
	v_readlane_b32 s74, v254, 8
	v_readlane_b32 s75, v254, 9
.LBB0_610:
	v_add_u32_e32 v226, s65, v185
	ds_read_b128 v[228:231], v226
	ds_read_b128 v[232:235], v226 offset:16
	ds_read_b128 v[236:239], v226 offset:32
	ds_read_b128 v[240:243], v226 offset:48
	ds_read_b128 v[2:5], v188
	ds_read_b128 v[10:13], v188 offset:2048
	ds_read_b128 v[6:9], v189
	ds_read_b128 v[14:17], v189 offset:2048
	ds_read_b128 v[18:21], v190
	ds_read_b128 v[26:29], v190 offset:2048
	ds_read_b128 v[22:25], v191
	ds_read_b128 v[30:33], v191 offset:2048
	s_ashr_i32 s35, s34, 31
	s_lshl_b64 s[6:7], s[34:35], 19
	s_add_u32 s36, s46, s6
	s_addc_u32 s37, s47, s7
	s_and_b64 s[4:5], s[4:5], exec
	s_cselect_b32 s35, s37, s41
	s_cselect_b32 s66, s36, s40
	s_add_i32 s67, s39, 0xc000
	s_mov_b32 m0, s67
	s_add_i32 s68, s39, 0xe000
	ds_read_b128 v[38:41], v192
	ds_read_b128 v[42:45], v192 offset:1024
	ds_read_b128 v[46:49], v192 offset:2048
	ds_read_b128 v[50:53], v192 offset:3072
	ds_read_b128 v[54:57], v192 offset:4096
	ds_read_b128 v[58:61], v192 offset:5120
	ds_read_b128 v[62:65], v192 offset:6144
	ds_read_b128 v[66:69], v192 offset:7168
	global_load_lds_dwordx4 v172, s[18:19]
	s_mov_b32 m0, s68
	v_mov_b32_e32 v173, v169
	global_load_lds_dwordx4 v174, s[18:19]
	s_waitcnt vmcnt(8)
	s_waitcnt lgkmcnt(0)
	v_mov_b32_e32 v175, v169
	s_barrier
	s_setprio 1
	s_mov_b32 s4, 0
	s_mov_b32 s6, s4
	s_mov_b32 s7, s4
	s_mov_b32 s5, s4
	s_waitcnt lgkmcnt(0)
	v_mfma_scale_f32_16x16x128_f8f6f4 v[158:161], v[2:9], v[38:45], v[228:231], v193, v194 op_sel_hi:[0,0,0]
	v_mfma_scale_f32_16x16x128_f8f6f4 v[154:157], v[10:17], v[38:45], v[232:235], v193, v194 op_sel_hi:[0,0,0]
	v_mfma_scale_f32_16x16x128_f8f6f4 v[142:145], v[2:9], v[46:53], v[228:231], v193, v194 op_sel_hi:[0,0,0]
	v_mfma_scale_f32_16x16x128_f8f6f4 v[138:141], v[10:17], v[46:53], v[232:235], v193, v194 op_sel_hi:[0,0,0]
	v_mfma_scale_f32_16x16x128_f8f6f4 v[126:129], v[2:9], v[54:61], v[228:231], v193, v194 op_sel_hi:[0,0,0]
	v_mfma_scale_f32_16x16x128_f8f6f4 v[122:125], v[10:17], v[54:61], v[232:235], v193, v194 op_sel_hi:[0,0,0]
	v_mfma_scale_f32_16x16x128_f8f6f4 v[110:113], v[2:9], v[62:69], v[228:231], v193, v194 op_sel_hi:[0,0,0]
	v_mfma_scale_f32_16x16x128_f8f6f4 v[106:109], v[10:17], v[62:69], v[232:235], v193, v194 op_sel_hi:[0,0,0]
	s_setprio 0
	s_setprio 1
	v_mfma_scale_f32_16x16x128_f8f6f4 v[150:153], v[18:25], v[38:45], v[236:239], v193, v194 op_sel_hi:[0,0,0]
	v_mfma_scale_f32_16x16x128_f8f6f4 v[146:149], v[26:33], v[38:45], v[240:243], v193, v194 op_sel_hi:[0,0,0]
	v_mfma_scale_f32_16x16x128_f8f6f4 v[134:137], v[18:25], v[46:53], v[236:239], v193, v194 op_sel_hi:[0,0,0]
	v_mfma_scale_f32_16x16x128_f8f6f4 v[130:133], v[26:33], v[46:53], v[240:243], v193, v194 op_sel_hi:[0,0,0]
	v_mfma_scale_f32_16x16x128_f8f6f4 v[118:121], v[18:25], v[54:61], v[236:239], v193, v194 op_sel_hi:[0,0,0]
	v_mfma_scale_f32_16x16x128_f8f6f4 v[114:117], v[26:33], v[54:61], v[240:243], v193, v194 op_sel_hi:[0,0,0]
	v_mfma_scale_f32_16x16x128_f8f6f4 v[98:101], v[18:25], v[62:69], v[236:239], v193, v194 op_sel_hi:[0,0,0]
	v_mfma_scale_f32_16x16x128_f8f6f4 v[90:93], v[26:33], v[62:69], v[240:243], v193, v194 op_sel_hi:[0,0,0]
	s_setprio 0
	s_barrier
	s_add_i32 s5, s56, s48
	v_lshl_add_u64 v[176:177], s[40:41], 0, v[166:167]
	s_add_i32 s69, s5, 0x2000
	v_lshl_add_u64 v[38:39], v[176:177], 0, s[28:29]
	s_mov_b32 m0, s5
	v_lshl_add_u64 v[178:179], s[40:41], 0, v[164:165]
	s_add_u32 s6, s40, 0x4100
	ds_read_b128 v[50:53], v192 offset:16384
	ds_read_b128 v[54:57], v192 offset:17408
	ds_read_b128 v[202:205], v192 offset:18432
	ds_read_b128 v[206:209], v192 offset:19456
	ds_read_b128 v[210:213], v192 offset:20480
	ds_read_b128 v[214:217], v192 offset:21504
	ds_read_b128 v[218:221], v192 offset:22528
	ds_read_b128 v[222:225], v192 offset:23552
	global_load_lds_dwordx4 v[38:39], off
	v_lshl_add_u64 v[38:39], v[178:179], 0, s[28:29]
	s_mov_b32 m0, s69
	s_addc_u32 s7, s41, 0
	s_add_i32 s70, s57, s48
	global_load_lds_dwordx4 v[38:39], off
	v_lshl_add_u64 v[38:39], s[6:7], 0, v[166:167]
	s_mov_b32 m0, s70
	s_add_i32 s71, s70, 0x2000
	global_load_lds_dwordx4 v[38:39], off
	v_lshl_add_u64 v[38:39], s[6:7], 0, v[164:165]
	s_mov_b32 m0, s71
	s_nop 0
	global_load_lds_dwordx4 v[38:39], off
	s_mov_b32 m0, s39
	s_nop 0
	global_load_lds_dwordx4 v200, s[24:25]
	s_mov_b32 m0, s51
	s_nop 0
	global_load_lds_dwordx4 v170, s[24:25]
	s_waitcnt vmcnt(8)
	s_waitcnt lgkmcnt(0)
	s_barrier
	s_setprio 1
	s_waitcnt lgkmcnt(0)
	v_mfma_scale_f32_16x16x128_f8f6f4 v[102:105], v[2:9], v[50:57], v[228:231], v193, v194 op_sel_hi:[0,0,0]
	v_mfma_scale_f32_16x16x128_f8f6f4 v[94:97], v[10:17], v[50:57], v[232:235], v193, v194 op_sel_hi:[0,0,0]
	v_mfma_scale_f32_16x16x128_f8f6f4 v[78:81], v[2:9], v[202:209], v[228:231], v193, v194 op_sel_hi:[0,0,0]
	v_mfma_scale_f32_16x16x128_f8f6f4 v[74:77], v[10:17], v[202:209], v[232:235], v193, v194 op_sel_hi:[0,0,0]
	v_mfma_scale_f32_16x16x128_f8f6f4 v[62:65], v[2:9], v[210:217], v[228:231], v193, v194 op_sel_hi:[0,0,0]
	v_mfma_scale_f32_16x16x128_f8f6f4 v[58:61], v[10:17], v[210:217], v[232:235], v193, v194 op_sel_hi:[0,0,0]
	v_mfma_scale_f32_16x16x128_f8f6f4 v[46:49], v[2:9], v[218:225], v[228:231], v193, v194 op_sel_hi:[0,0,0]
	v_mfma_scale_f32_16x16x128_f8f6f4 v[42:45], v[10:17], v[218:225], v[232:235], v193, v194 op_sel_hi:[0,0,0]
	s_setprio 0
	s_setprio 1
	v_mfma_scale_f32_16x16x128_f8f6f4 v[86:89], v[18:25], v[50:57], v[236:239], v193, v194 op_sel_hi:[0,0,0]
	v_mfma_scale_f32_16x16x128_f8f6f4 v[82:85], v[26:33], v[50:57], v[240:243], v193, v194 op_sel_hi:[0,0,0]
	v_mfma_scale_f32_16x16x128_f8f6f4 v[70:73], v[18:25], v[202:209], v[236:239], v193, v194 op_sel_hi:[0,0,0]
	v_mfma_scale_f32_16x16x128_f8f6f4 v[66:69], v[26:33], v[202:209], v[240:243], v193, v194 op_sel_hi:[0,0,0]
	v_mfma_scale_f32_16x16x128_f8f6f4 v[54:57], v[18:25], v[210:217], v[236:239], v193, v194 op_sel_hi:[0,0,0]
	v_mfma_scale_f32_16x16x128_f8f6f4 v[50:53], v[26:33], v[210:217], v[240:243], v193, v194 op_sel_hi:[0,0,0]
	v_mfma_scale_f32_16x16x128_f8f6f4 v[38:41], v[18:25], v[218:225], v[236:239], v193, v194 op_sel_hi:[0,0,0]
	v_mfma_scale_f32_16x16x128_f8f6f4 v[34:37], v[26:33], v[218:225], v[240:243], v193, v194 op_sel_hi:[0,0,0]
	s_setprio 0
	s_barrier
	s_add_i32 s72, 0, 0x18000
	s_add_i32 s74, 0, 0x1c000
	v_add_u32_e32 v201, s72, v171
	v_add_u32_e32 v203, s74, v171
	v_add_u32_e32 v202, s72, v182
	ds_read_b128 v[18:21], v201
	ds_read_b128 v[26:29], v201 offset:2048
	ds_read_b128 v[22:25], v202
	ds_read_b128 v[30:33], v202 offset:2048
	v_add_u32_e32 v204, s74, v182
	ds_read_b128 v[2:5], v203
	ds_read_b128 v[10:13], v203 offset:2048
	ds_read_b128 v[6:9], v204
	ds_read_b128 v[14:17], v204 offset:2048
	s_mov_b32 m0, s52
	ds_read_b128 v[206:209], v192 offset:32768
	ds_read_b128 v[210:213], v192 offset:33792
	ds_read_b128 v[214:217], v192 offset:34816
	ds_read_b128 v[218:221], v192 offset:35840
	ds_read_b128 v[222:225], v192 offset:36864
	ds_read_b128 v[226:229], v192 offset:37888
	ds_read_b128 v[230:233], v192 offset:38912
	ds_read_b128 v[234:237], v192 offset:39936
	global_load_lds_dwordx4 v172, s[24:25]
	s_mov_b32 m0, s53
	s_nop 0
	global_load_lds_dwordx4 v174, s[24:25]
	s_waitcnt vmcnt(8)
	s_waitcnt lgkmcnt(0)
	s_barrier
	s_setprio 1
	s_waitcnt lgkmcnt(0)
	v_mfma_scale_f32_16x16x128_f8f6f4 v[158:161], v[18:25], v[206:213], v[158:161], v193, v194 op_sel_hi:[0,0,0]
	v_mfma_scale_f32_16x16x128_f8f6f4 v[154:157], v[26:33], v[206:213], v[154:157], v193, v194 op_sel_hi:[0,0,0]
	v_mfma_scale_f32_16x16x128_f8f6f4 v[142:145], v[18:25], v[214:221], v[142:145], v193, v194 op_sel_hi:[0,0,0]
	v_mfma_scale_f32_16x16x128_f8f6f4 v[138:141], v[26:33], v[214:221], v[138:141], v193, v194 op_sel_hi:[0,0,0]
	v_mfma_scale_f32_16x16x128_f8f6f4 v[126:129], v[18:25], v[222:229], v[126:129], v193, v194 op_sel_hi:[0,0,0]
	v_mfma_scale_f32_16x16x128_f8f6f4 v[122:125], v[26:33], v[222:229], v[122:125], v193, v194 op_sel_hi:[0,0,0]
	v_mfma_scale_f32_16x16x128_f8f6f4 v[110:113], v[18:25], v[230:237], v[110:113], v193, v194 op_sel_hi:[0,0,0]
	v_mfma_scale_f32_16x16x128_f8f6f4 v[106:109], v[26:33], v[230:237], v[106:109], v193, v194 op_sel_hi:[0,0,0]
	s_setprio 0
	s_setprio 1
	v_mfma_scale_f32_16x16x128_f8f6f4 v[150:153], v[2:9], v[206:213], v[150:153], v193, v194 op_sel_hi:[0,0,0]
	v_mfma_scale_f32_16x16x128_f8f6f4 v[146:149], v[10:17], v[206:213], v[146:149], v193, v194 op_sel_hi:[0,0,0]
	v_mfma_scale_f32_16x16x128_f8f6f4 v[134:137], v[2:9], v[214:221], v[134:137], v193, v194 op_sel_hi:[0,0,0]
	v_mfma_scale_f32_16x16x128_f8f6f4 v[130:133], v[10:17], v[214:221], v[130:133], v193, v194 op_sel_hi:[0,0,0]
	v_mfma_scale_f32_16x16x128_f8f6f4 v[118:121], v[2:9], v[222:229], v[118:121], v193, v194 op_sel_hi:[0,0,0]
	v_mfma_scale_f32_16x16x128_f8f6f4 v[114:117], v[10:17], v[222:229], v[114:117], v193, v194 op_sel_hi:[0,0,0]
	v_mfma_scale_f32_16x16x128_f8f6f4 v[98:101], v[2:9], v[230:237], v[98:101], v193, v194 op_sel_hi:[0,0,0]
	v_mfma_scale_f32_16x16x128_f8f6f4 v[90:93], v[10:17], v[230:237], v[90:93], v193, v194 op_sel_hi:[0,0,0]
	s_setprio 0
	s_barrier
	s_add_i32 s72, s72, s48
	s_add_i32 s73, s72, 0x2000
	v_lshl_add_u64 v[176:177], v[176:177], 0, s[30:31]
	s_mov_b32 m0, s72
	s_add_u32 s6, s40, 0x4180
	ds_read_b128 v[206:209], v192 offset:49152
	ds_read_b128 v[210:213], v192 offset:50176
	ds_read_b128 v[214:217], v192 offset:51200
	ds_read_b128 v[218:221], v192 offset:52224
	ds_read_b128 v[222:225], v192 offset:53248
	ds_read_b128 v[226:229], v192 offset:54272
	ds_read_b128 v[230:233], v192 offset:55296
	ds_read_b128 v[234:237], v192 offset:56320
	global_load_lds_dwordx4 v[176:177], off
	v_lshl_add_u64 v[176:177], v[178:179], 0, s[30:31]
	s_mov_b32 m0, s73
	s_addc_u32 s7, s41, 0
	s_add_i32 s74, s74, s48
	global_load_lds_dwordx4 v[176:177], off
	v_lshl_add_u64 v[176:177], s[6:7], 0, v[166:167]
	s_mov_b32 m0, s74
	s_add_i32 s75, s74, 0x2000
	global_load_lds_dwordx4 v[176:177], off
	v_lshl_add_u64 v[176:177], s[6:7], 0, v[164:165]
	s_mov_b32 m0, s75
	s_nop 0
	global_load_lds_dwordx4 v[176:177], off
	s_mov_b32 m0, s54
	s_nop 0
	global_load_lds_dwordx4 v200, s[26:27]
	s_mov_b32 m0, s55
	s_nop 0
	global_load_lds_dwordx4 v170, s[26:27]
	s_waitcnt vmcnt(8)
	s_waitcnt lgkmcnt(0)
	s_barrier
	s_setprio 1
	s_waitcnt lgkmcnt(0)
	v_mfma_scale_f32_16x16x128_f8f6f4 v[102:105], v[18:25], v[206:213], v[102:105], v193, v194 op_sel_hi:[0,0,0]
	v_mfma_scale_f32_16x16x128_f8f6f4 v[94:97], v[26:33], v[206:213], v[94:97], v193, v194 op_sel_hi:[0,0,0]
	v_mfma_scale_f32_16x16x128_f8f6f4 v[78:81], v[18:25], v[214:221], v[78:81], v193, v194 op_sel_hi:[0,0,0]
	v_mfma_scale_f32_16x16x128_f8f6f4 v[74:77], v[26:33], v[214:221], v[74:77], v193, v194 op_sel_hi:[0,0,0]
	v_mfma_scale_f32_16x16x128_f8f6f4 v[62:65], v[18:25], v[222:229], v[62:65], v193, v194 op_sel_hi:[0,0,0]
	v_mfma_scale_f32_16x16x128_f8f6f4 v[58:61], v[26:33], v[222:229], v[58:61], v193, v194 op_sel_hi:[0,0,0]
	v_mfma_scale_f32_16x16x128_f8f6f4 v[46:49], v[18:25], v[230:237], v[46:49], v193, v194 op_sel_hi:[0,0,0]
	v_mfma_scale_f32_16x16x128_f8f6f4 v[42:45], v[26:33], v[230:237], v[42:45], v193, v194 op_sel_hi:[0,0,0]
	s_setprio 0
	s_setprio 1
	v_mfma_scale_f32_16x16x128_f8f6f4 v[86:89], v[2:9], v[206:213], v[86:89], v193, v194 op_sel_hi:[0,0,0]
	v_mfma_scale_f32_16x16x128_f8f6f4 v[82:85], v[10:17], v[206:213], v[82:85], v193, v194 op_sel_hi:[0,0,0]
	v_mfma_scale_f32_16x16x128_f8f6f4 v[70:73], v[2:9], v[214:221], v[70:73], v193, v194 op_sel_hi:[0,0,0]
	v_mfma_scale_f32_16x16x128_f8f6f4 v[66:69], v[10:17], v[214:221], v[66:69], v193, v194 op_sel_hi:[0,0,0]
	v_mfma_scale_f32_16x16x128_f8f6f4 v[54:57], v[2:9], v[222:229], v[54:57], v193, v194 op_sel_hi:[0,0,0]
	v_mfma_scale_f32_16x16x128_f8f6f4 v[50:53], v[10:17], v[222:229], v[50:53], v193, v194 op_sel_hi:[0,0,0]
	v_mfma_scale_f32_16x16x128_f8f6f4 v[38:41], v[2:9], v[230:237], v[38:41], v193, v194 op_sel_hi:[0,0,0]
	v_mfma_scale_f32_16x16x128_f8f6f4 v[34:37], v[10:17], v[230:237], v[34:37], v193, v194 op_sel_hi:[0,0,0]
	s_setprio 0
	s_barrier
	s_add_u32 s76, s40, 0x200
	v_lshl_add_u64 v[18:19], s[26:27], 0, v[174:175]
	v_lshl_add_u64 v[20:21], s[26:27], 0, v[172:173]
	s_addc_u32 s77, s41, 0
	s_mov_b64 s[6:7], 0

.LBB0_614:
	s_nop 15
	s_nop 15
	v_lshl_add_u32 v20, s64, 8, v184
	s_waitcnt lgkmcnt(0)
	v_mov_b32_e32 v226, 1.0
	v_mov_b32_e32 v227, 1.0
	v_min_f32_e32 v158, 0x40e00000, v158
	v_min_f32_e32 v160, 0x40e00000, v160
	v_min_f32_e32 v154, 0x40e00000, v154
	v_min_f32_e32 v156, 0x40e00000, v156
	v_min_f32_e32 v150, 0x40e00000, v150
	v_min_f32_e32 v152, 0x40e00000, v152
	v_min_f32_e32 v146, 0x40e00000, v146
	v_min_f32_e32 v148, 0x40e00000, v148
	v_mul_f32_e32 v206, 0xc01d265f, v158
	v_mul_f32_e32 v208, 0xc01d265f, v160
	v_mul_f32_e32 v210, 0xc01d265f, v154
	v_mul_f32_e32 v212, 0xc01d265f, v156
	v_mul_f32_e32 v214, 0xc01d265f, v150
	v_mul_f32_e32 v216, 0xc01d265f, v152
	v_mul_f32_e32 v218, 0xc01d265f, v146
	v_mul_f32_e32 v220, 0xc01d265f, v148
	v_exp_f32_e32 v206, v206
	v_exp_f32_e32 v208, v208
	v_exp_f32_e32 v210, v210
	v_exp_f32_e32 v212, v212
	v_exp_f32_e32 v214, v214
	v_exp_f32_e32 v216, v216
	v_exp_f32_e32 v218, v218
	v_exp_f32_e32 v220, v220
	v_med3_f32 v207, v159, s58, v195
	v_med3_f32 v209, v161, s58, v195
	v_med3_f32 v211, v155, s58, v195
	v_med3_f32 v213, v157, s58, v195
	v_med3_f32 v215, v151, s58, v195
	v_med3_f32 v217, v153, s58, v195
	v_med3_f32 v219, v147, s58, v195
	v_med3_f32 v221, v149, s58, v195
	v_pk_add_f32 v[206:207], v[206:207], v[226:227]
	v_pk_add_f32 v[208:209], v[208:209], v[226:227]
	v_pk_add_f32 v[210:211], v[210:211], v[226:227]
	v_pk_add_f32 v[212:213], v[212:213], v[226:227]
	v_pk_add_f32 v[214:215], v[214:215], v[226:227]
	v_pk_add_f32 v[216:217], v[216:217], v[226:227]
	v_pk_add_f32 v[218:219], v[218:219], v[226:227]
	v_pk_add_f32 v[220:221], v[220:221], v[226:227]
	v_rcp_f32_e32 v206, v206
	v_rcp_f32_e32 v208, v208
	v_rcp_f32_e32 v210, v210
	v_rcp_f32_e32 v212, v212
	v_rcp_f32_e32 v214, v214
	v_rcp_f32_e32 v216, v216
	v_rcp_f32_e32 v218, v218
	v_rcp_f32_e32 v220, v220
	v_mul_f32_e32 v158, v158, v206
	v_mul_f32_e32 v160, v160, v208
	v_mul_f32_e32 v154, v154, v210
	v_mul_f32_e32 v156, v156, v212
	v_mul_f32_e32 v150, v150, v214
	v_mul_f32_e32 v152, v152, v216
	v_mul_f32_e32 v146, v146, v218
	v_mul_f32_e32 v148, v148, v220
	v_mul_f32_e32 v158, v207, v158
	v_mul_f32_e32 v160, v209, v160
	v_mul_f32_e32 v154, v211, v154
	v_mul_f32_e32 v156, v213, v156
	v_mul_f32_e32 v150, v215, v150
	v_mul_f32_e32 v152, v217, v152
	v_mul_f32_e32 v146, v219, v146
	v_mul_f32_e32 v148, v221, v148
	v_cvt_pk_fp8_f32 v222, v158, v160
	v_cvt_pk_fp8_f32 v223, v150, v152
	s_lshl_b32 s4, s38, 7
	v_ashrrev_i32_e32 v21, 31, v20
	s_and_b32 s4, s4, 0x780
	v_lshlrev_b64 v[18:19], 11, v[20:21]
	v_or_b32_e32 v168, s4, v183
	v_lshl_add_u64 v[18:19], s[14:15], 0, v[18:19]
	v_lshl_add_u64 v[18:19], v[18:19], 0, v[168:169]
	v_cvt_pk_fp8_f32 v222, v154, v156 op_sel:[0,0,1]
	v_cvt_pk_fp8_f32 v223, v146, v148 op_sel:[0,0,1]
	global_store_dwordx2 v[18:19], v[222:223], off
	v_min_f32_e32 v142, 0x40e00000, v142
	v_min_f32_e32 v144, 0x40e00000, v144
	v_min_f32_e32 v138, 0x40e00000, v138
	v_min_f32_e32 v140, 0x40e00000, v140
	v_min_f32_e32 v134, 0x40e00000, v134
	v_min_f32_e32 v136, 0x40e00000, v136
	v_min_f32_e32 v130, 0x40e00000, v130
	v_min_f32_e32 v132, 0x40e00000, v132
	v_mul_f32_e32 v206, 0xc01d265f, v142
	v_mul_f32_e32 v208, 0xc01d265f, v144
	v_mul_f32_e32 v210, 0xc01d265f, v138
	v_mul_f32_e32 v212, 0xc01d265f, v140
	v_mul_f32_e32 v214, 0xc01d265f, v134
	v_mul_f32_e32 v216, 0xc01d265f, v136
	v_mul_f32_e32 v218, 0xc01d265f, v130
	v_mul_f32_e32 v220, 0xc01d265f, v132
	v_exp_f32_e32 v206, v206
	v_exp_f32_e32 v208, v208
	v_exp_f32_e32 v210, v210
	v_exp_f32_e32 v212, v212
	v_exp_f32_e32 v214, v214
	v_exp_f32_e32 v216, v216
	v_exp_f32_e32 v218, v218
	v_exp_f32_e32 v220, v220
	v_med3_f32 v207, v143, s58, v195
	v_med3_f32 v209, v145, s58, v195
	v_med3_f32 v211, v139, s58, v195
	v_med3_f32 v213, v141, s58, v195
	v_med3_f32 v215, v135, s58, v195
	v_med3_f32 v217, v137, s58, v195
	v_med3_f32 v219, v131, s58, v195
	v_med3_f32 v221, v133, s58, v195
	v_pk_add_f32 v[206:207], v[206:207], v[226:227]
	v_pk_add_f32 v[208:209], v[208:209], v[226:227]
	v_pk_add_f32 v[210:211], v[210:211], v[226:227]
	v_pk_add_f32 v[212:213], v[212:213], v[226:227]
	v_pk_add_f32 v[214:215], v[214:215], v[226:227]
	v_pk_add_f32 v[216:217], v[216:217], v[226:227]
	v_pk_add_f32 v[218:219], v[218:219], v[226:227]
	v_pk_add_f32 v[220:221], v[220:221], v[226:227]
	v_rcp_f32_e32 v206, v206
	v_rcp_f32_e32 v208, v208
	v_rcp_f32_e32 v210, v210
	v_rcp_f32_e32 v212, v212
	v_rcp_f32_e32 v214, v214
	v_rcp_f32_e32 v216, v216
	v_rcp_f32_e32 v218, v218
	v_rcp_f32_e32 v220, v220
	v_mul_f32_e32 v142, v142, v206
	v_mul_f32_e32 v144, v144, v208
	v_mul_f32_e32 v138, v138, v210
	v_mul_f32_e32 v140, v140, v212
	v_mul_f32_e32 v134, v134, v214
	v_mul_f32_e32 v136, v136, v216
	v_mul_f32_e32 v130, v130, v218
	v_mul_f32_e32 v132, v132, v220
	v_mul_f32_e32 v142, v207, v142
	v_mul_f32_e32 v144, v209, v144
	v_mul_f32_e32 v138, v211, v138
	v_mul_f32_e32 v140, v213, v140
	v_mul_f32_e32 v134, v215, v134
	v_mul_f32_e32 v136, v217, v136
	v_mul_f32_e32 v130, v219, v130
	v_mul_f32_e32 v132, v221, v132
	v_cvt_pk_fp8_f32 v222, v142, v144
	v_cvt_pk_fp8_f32 v223, v134, v136
	v_or_b32_e32 v224, 16, v20
	v_ashrrev_i32_e32 v225, 31, v224
	v_lshlrev_b64 v[224:225], 11, v[224:225]
	v_lshl_add_u64 v[224:225], s[14:15], 0, v[224:225]
	v_lshl_add_u64 v[224:225], v[224:225], 0, v[168:169]
	v_cvt_pk_fp8_f32 v222, v138, v140 op_sel:[0,0,1]
	v_cvt_pk_fp8_f32 v223, v130, v132 op_sel:[0,0,1]
	global_store_dwordx2 v[224:225], v[222:223], off
	v_min_f32_e32 v126, 0x40e00000, v126
	v_min_f32_e32 v128, 0x40e00000, v128
	v_min_f32_e32 v122, 0x40e00000, v122
	v_min_f32_e32 v124, 0x40e00000, v124
	v_min_f32_e32 v118, 0x40e00000, v118
	v_min_f32_e32 v120, 0x40e00000, v120
	v_min_f32_e32 v114, 0x40e00000, v114
	v_min_f32_e32 v116, 0x40e00000, v116
	v_mul_f32_e32 v206, 0xc01d265f, v126
	v_mul_f32_e32 v208, 0xc01d265f, v128
	v_mul_f32_e32 v210, 0xc01d265f, v122
	v_mul_f32_e32 v212, 0xc01d265f, v124
	v_mul_f32_e32 v214, 0xc01d265f, v118
	v_mul_f32_e32 v216, 0xc01d265f, v120
	v_mul_f32_e32 v218, 0xc01d265f, v114
	v_mul_f32_e32 v220, 0xc01d265f, v116
	v_exp_f32_e32 v206, v206
	v_exp_f32_e32 v208, v208
	v_exp_f32_e32 v210, v210
	v_exp_f32_e32 v212, v212
	v_exp_f32_e32 v214, v214
	v_exp_f32_e32 v216, v216
	v_exp_f32_e32 v218, v218
	v_exp_f32_e32 v220, v220
	v_med3_f32 v207, v127, s58, v195
	v_med3_f32 v209, v129, s58, v195
	v_med3_f32 v211, v123, s58, v195
	v_med3_f32 v213, v125, s58, v195
	v_med3_f32 v215, v119, s58, v195
	v_med3_f32 v217, v121, s58, v195
	v_med3_f32 v219, v115, s58, v195
	v_med3_f32 v221, v117, s58, v195
	v_pk_add_f32 v[206:207], v[206:207], v[226:227]
	v_pk_add_f32 v[208:209], v[208:209], v[226:227]
	v_pk_add_f32 v[210:211], v[210:211], v[226:227]
	v_pk_add_f32 v[212:213], v[212:213], v[226:227]
	v_pk_add_f32 v[214:215], v[214:215], v[226:227]
	v_pk_add_f32 v[216:217], v[216:217], v[226:227]
	v_pk_add_f32 v[218:219], v[218:219], v[226:227]
	v_pk_add_f32 v[220:221], v[220:221], v[226:227]
	v_rcp_f32_e32 v206, v206
	v_rcp_f32_e32 v208, v208
	v_rcp_f32_e32 v210, v210
	v_rcp_f32_e32 v212, v212
	v_rcp_f32_e32 v214, v214
	v_rcp_f32_e32 v216, v216
	v_rcp_f32_e32 v218, v218
	v_rcp_f32_e32 v220, v220
	v_mul_f32_e32 v126, v126, v206
	v_mul_f32_e32 v128, v128, v208
	v_mul_f32_e32 v122, v122, v210
	v_mul_f32_e32 v124, v124, v212
	v_mul_f32_e32 v118, v118, v214
	v_mul_f32_e32 v120, v120, v216
	v_mul_f32_e32 v114, v114, v218
	v_mul_f32_e32 v116, v116, v220
	v_mul_f32_e32 v126, v207, v126
	v_mul_f32_e32 v128, v209, v128
	v_mul_f32_e32 v122, v211, v122
	v_mul_f32_e32 v124, v213, v124
	v_mul_f32_e32 v118, v215, v118
	v_mul_f32_e32 v120, v217, v120
	v_mul_f32_e32 v114, v219, v114
	v_mul_f32_e32 v116, v221, v116
	v_cvt_pk_fp8_f32 v222, v126, v128
	v_cvt_pk_fp8_f32 v223, v118, v120
	v_or_b32_e32 v224, 32, v20
	v_ashrrev_i32_e32 v225, 31, v224
	v_lshlrev_b64 v[224:225], 11, v[224:225]
	v_lshl_add_u64 v[224:225], s[14:15], 0, v[224:225]
	v_lshl_add_u64 v[224:225], v[224:225], 0, v[168:169]
	v_cvt_pk_fp8_f32 v222, v122, v124 op_sel:[0,0,1]
	v_cvt_pk_fp8_f32 v223, v114, v116 op_sel:[0,0,1]
	global_store_dwordx2 v[224:225], v[222:223], off
	v_min_f32_e32 v110, 0x40e00000, v110
	v_min_f32_e32 v112, 0x40e00000, v112
	v_min_f32_e32 v106, 0x40e00000, v106
	v_min_f32_e32 v108, 0x40e00000, v108
	v_min_f32_e32 v98, 0x40e00000, v98
	v_min_f32_e32 v100, 0x40e00000, v100
	v_min_f32_e32 v90, 0x40e00000, v90
	v_min_f32_e32 v92, 0x40e00000, v92
	v_mul_f32_e32 v206, 0xc01d265f, v110
	v_mul_f32_e32 v208, 0xc01d265f, v112
	v_mul_f32_e32 v210, 0xc01d265f, v106
	v_mul_f32_e32 v212, 0xc01d265f, v108
	v_mul_f32_e32 v214, 0xc01d265f, v98
	v_mul_f32_e32 v216, 0xc01d265f, v100
	v_mul_f32_e32 v218, 0xc01d265f, v90
	v_mul_f32_e32 v220, 0xc01d265f, v92
	v_exp_f32_e32 v206, v206
	v_exp_f32_e32 v208, v208
	v_exp_f32_e32 v210, v210
	v_exp_f32_e32 v212, v212
	v_exp_f32_e32 v214, v214
	v_exp_f32_e32 v216, v216
	v_exp_f32_e32 v218, v218
	v_exp_f32_e32 v220, v220
	v_med3_f32 v207, v111, s58, v195
	v_med3_f32 v209, v113, s58, v195
	v_med3_f32 v211, v107, s58, v195
	v_med3_f32 v213, v109, s58, v195
	v_med3_f32 v215, v99, s58, v195
	v_med3_f32 v217, v101, s58, v195
	v_med3_f32 v219, v91, s58, v195
	v_med3_f32 v221, v93, s58, v195
	v_pk_add_f32 v[206:207], v[206:207], v[226:227]
	v_pk_add_f32 v[208:209], v[208:209], v[226:227]
	v_pk_add_f32 v[210:211], v[210:211], v[226:227]
	v_pk_add_f32 v[212:213], v[212:213], v[226:227]
	v_pk_add_f32 v[214:215], v[214:215], v[226:227]
	v_pk_add_f32 v[216:217], v[216:217], v[226:227]
	v_pk_add_f32 v[218:219], v[218:219], v[226:227]
	v_pk_add_f32 v[220:221], v[220:221], v[226:227]
	v_rcp_f32_e32 v206, v206
	v_rcp_f32_e32 v208, v208
	v_rcp_f32_e32 v210, v210
	v_rcp_f32_e32 v212, v212
	v_rcp_f32_e32 v214, v214
	v_rcp_f32_e32 v216, v216
	v_rcp_f32_e32 v218, v218
	v_rcp_f32_e32 v220, v220
	v_mul_f32_e32 v110, v110, v206
	v_mul_f32_e32 v112, v112, v208
	v_mul_f32_e32 v106, v106, v210
	v_mul_f32_e32 v108, v108, v212
	v_mul_f32_e32 v98, v98, v214
	v_mul_f32_e32 v100, v100, v216
	v_mul_f32_e32 v90, v90, v218
	v_mul_f32_e32 v92, v92, v220
	v_mul_f32_e32 v110, v207, v110
	v_mul_f32_e32 v112, v209, v112
	v_mul_f32_e32 v106, v211, v106
	v_mul_f32_e32 v108, v213, v108
	v_mul_f32_e32 v98, v215, v98
	v_mul_f32_e32 v100, v217, v100
	v_mul_f32_e32 v90, v219, v90
	v_mul_f32_e32 v92, v221, v92
	v_cvt_pk_fp8_f32 v222, v110, v112
	v_cvt_pk_fp8_f32 v223, v98, v100
	v_or_b32_e32 v224, 48, v20
	v_ashrrev_i32_e32 v225, 31, v224
	v_lshlrev_b64 v[224:225], 11, v[224:225]
	v_lshl_add_u64 v[224:225], s[14:15], 0, v[224:225]
	v_lshl_add_u64 v[224:225], v[224:225], 0, v[168:169]
	v_cvt_pk_fp8_f32 v222, v106, v108 op_sel:[0,0,1]
	v_cvt_pk_fp8_f32 v223, v90, v92 op_sel:[0,0,1]
	global_store_dwordx2 v[224:225], v[222:223], off
	v_min_f32_e32 v102, 0x40e00000, v102
	v_min_f32_e32 v104, 0x40e00000, v104
	v_min_f32_e32 v94, 0x40e00000, v94
	v_min_f32_e32 v96, 0x40e00000, v96
	v_min_f32_e32 v86, 0x40e00000, v86
	v_min_f32_e32 v88, 0x40e00000, v88
	v_min_f32_e32 v82, 0x40e00000, v82
	v_min_f32_e32 v84, 0x40e00000, v84
	v_mul_f32_e32 v206, 0xc01d265f, v102
	v_mul_f32_e32 v208, 0xc01d265f, v104
	v_mul_f32_e32 v210, 0xc01d265f, v94
	v_mul_f32_e32 v212, 0xc01d265f, v96
	v_mul_f32_e32 v214, 0xc01d265f, v86
	v_mul_f32_e32 v216, 0xc01d265f, v88
	v_mul_f32_e32 v218, 0xc01d265f, v82
	v_mul_f32_e32 v220, 0xc01d265f, v84
	v_exp_f32_e32 v206, v206
	v_exp_f32_e32 v208, v208
	v_exp_f32_e32 v210, v210
	v_exp_f32_e32 v212, v212
	v_exp_f32_e32 v214, v214
	v_exp_f32_e32 v216, v216
	v_exp_f32_e32 v218, v218
	v_exp_f32_e32 v220, v220
	v_med3_f32 v207, v103, s58, v195
	v_med3_f32 v209, v105, s58, v195
	v_med3_f32 v211, v95, s58, v195
	v_med3_f32 v213, v97, s58, v195
	v_med3_f32 v215, v87, s58, v195
	v_med3_f32 v217, v89, s58, v195
	v_med3_f32 v219, v83, s58, v195
	v_med3_f32 v221, v85, s58, v195
	v_pk_add_f32 v[206:207], v[206:207], v[226:227]
	v_pk_add_f32 v[208:209], v[208:209], v[226:227]
	v_pk_add_f32 v[210:211], v[210:211], v[226:227]
	v_pk_add_f32 v[212:213], v[212:213], v[226:227]
	v_pk_add_f32 v[214:215], v[214:215], v[226:227]
	v_pk_add_f32 v[216:217], v[216:217], v[226:227]
	v_pk_add_f32 v[218:219], v[218:219], v[226:227]
	v_pk_add_f32 v[220:221], v[220:221], v[226:227]
	v_rcp_f32_e32 v206, v206
	v_rcp_f32_e32 v208, v208
	v_rcp_f32_e32 v210, v210
	v_rcp_f32_e32 v212, v212
	v_rcp_f32_e32 v214, v214
	v_rcp_f32_e32 v216, v216
	v_rcp_f32_e32 v218, v218
	v_rcp_f32_e32 v220, v220
	v_mul_f32_e32 v102, v102, v206
	v_mul_f32_e32 v104, v104, v208
	v_mul_f32_e32 v94, v94, v210
	v_mul_f32_e32 v96, v96, v212
	v_mul_f32_e32 v86, v86, v214
	v_mul_f32_e32 v88, v88, v216
	v_mul_f32_e32 v82, v82, v218
	v_mul_f32_e32 v84, v84, v220
	v_mul_f32_e32 v102, v207, v102
	v_mul_f32_e32 v104, v209, v104
	v_mul_f32_e32 v94, v211, v94
	v_mul_f32_e32 v96, v213, v96
	v_mul_f32_e32 v86, v215, v86
	v_mul_f32_e32 v88, v217, v88
	v_mul_f32_e32 v82, v219, v82
	v_mul_f32_e32 v84, v221, v84
	v_cvt_pk_fp8_f32 v222, v102, v104
	v_cvt_pk_fp8_f32 v223, v86, v88
	v_add_co_u32_e32 v224, vcc, s59, v18
	s_nop 1
	v_addc_co_u32_e32 v225, vcc, 0, v19, vcc
	v_cvt_pk_fp8_f32 v222, v94, v96 op_sel:[0,0,1]
	v_cvt_pk_fp8_f32 v223, v82, v84 op_sel:[0,0,1]
	global_store_dwordx2 v[224:225], v[222:223], off
	v_min_f32_e32 v78, 0x40e00000, v78
	v_min_f32_e32 v80, 0x40e00000, v80
	v_min_f32_e32 v74, 0x40e00000, v74
	v_min_f32_e32 v76, 0x40e00000, v76
	v_min_f32_e32 v70, 0x40e00000, v70
	v_min_f32_e32 v72, 0x40e00000, v72
	v_min_f32_e32 v66, 0x40e00000, v66
	v_min_f32_e32 v68, 0x40e00000, v68
	v_mul_f32_e32 v206, 0xc01d265f, v78
	v_mul_f32_e32 v208, 0xc01d265f, v80
	v_mul_f32_e32 v210, 0xc01d265f, v74
	v_mul_f32_e32 v212, 0xc01d265f, v76
	v_mul_f32_e32 v214, 0xc01d265f, v70
	v_mul_f32_e32 v216, 0xc01d265f, v72
	v_mul_f32_e32 v218, 0xc01d265f, v66
	v_mul_f32_e32 v220, 0xc01d265f, v68
	v_exp_f32_e32 v206, v206
	v_exp_f32_e32 v208, v208
	v_exp_f32_e32 v210, v210
	v_exp_f32_e32 v212, v212
	v_exp_f32_e32 v214, v214
	v_exp_f32_e32 v216, v216
	v_exp_f32_e32 v218, v218
	v_exp_f32_e32 v220, v220
	v_med3_f32 v207, v79, s58, v195
	v_med3_f32 v209, v81, s58, v195
	v_med3_f32 v211, v75, s58, v195
	v_med3_f32 v213, v77, s58, v195
	v_med3_f32 v215, v71, s58, v195
	v_med3_f32 v217, v73, s58, v195
	v_med3_f32 v219, v67, s58, v195
	v_med3_f32 v221, v69, s58, v195
	v_pk_add_f32 v[206:207], v[206:207], v[226:227]
	v_pk_add_f32 v[208:209], v[208:209], v[226:227]
	v_pk_add_f32 v[210:211], v[210:211], v[226:227]
	v_pk_add_f32 v[212:213], v[212:213], v[226:227]
	v_pk_add_f32 v[214:215], v[214:215], v[226:227]
	v_pk_add_f32 v[216:217], v[216:217], v[226:227]
	v_pk_add_f32 v[218:219], v[218:219], v[226:227]
	v_pk_add_f32 v[220:221], v[220:221], v[226:227]
	v_rcp_f32_e32 v206, v206
	v_rcp_f32_e32 v208, v208
	v_rcp_f32_e32 v210, v210
	v_rcp_f32_e32 v212, v212
	v_rcp_f32_e32 v214, v214
	v_rcp_f32_e32 v216, v216
	v_rcp_f32_e32 v218, v218
	v_rcp_f32_e32 v220, v220
	v_mul_f32_e32 v78, v78, v206
	v_mul_f32_e32 v80, v80, v208
	v_mul_f32_e32 v74, v74, v210
	v_mul_f32_e32 v76, v76, v212
	v_mul_f32_e32 v70, v70, v214
	v_mul_f32_e32 v72, v72, v216
	v_mul_f32_e32 v66, v66, v218
	v_mul_f32_e32 v68, v68, v220
	v_mul_f32_e32 v78, v207, v78
	v_mul_f32_e32 v80, v209, v80
	v_mul_f32_e32 v74, v211, v74
	v_mul_f32_e32 v76, v213, v76
	v_mul_f32_e32 v70, v215, v70
	v_mul_f32_e32 v72, v217, v72
	v_mul_f32_e32 v66, v219, v66
	v_mul_f32_e32 v68, v221, v68
	v_cvt_pk_fp8_f32 v222, v78, v80
	v_cvt_pk_fp8_f32 v223, v70, v72
	v_add_co_u32_e32 v224, vcc, s60, v18
	s_nop 1
	v_addc_co_u32_e32 v225, vcc, 0, v19, vcc
	v_cvt_pk_fp8_f32 v222, v74, v76 op_sel:[0,0,1]
	v_cvt_pk_fp8_f32 v223, v66, v68 op_sel:[0,0,1]
	global_store_dwordx2 v[224:225], v[222:223], off
	v_min_f32_e32 v62, 0x40e00000, v62
	v_min_f32_e32 v64, 0x40e00000, v64
	v_min_f32_e32 v58, 0x40e00000, v58
	v_min_f32_e32 v60, 0x40e00000, v60
	v_min_f32_e32 v54, 0x40e00000, v54
	v_min_f32_e32 v56, 0x40e00000, v56
	v_min_f32_e32 v50, 0x40e00000, v50
	v_min_f32_e32 v52, 0x40e00000, v52
	v_mul_f32_e32 v206, 0xc01d265f, v62
	v_mul_f32_e32 v208, 0xc01d265f, v64
	v_mul_f32_e32 v210, 0xc01d265f, v58
	v_mul_f32_e32 v212, 0xc01d265f, v60
	v_mul_f32_e32 v214, 0xc01d265f, v54
	v_mul_f32_e32 v216, 0xc01d265f, v56
	v_mul_f32_e32 v218, 0xc01d265f, v50
	v_mul_f32_e32 v220, 0xc01d265f, v52
	v_exp_f32_e32 v206, v206
	v_exp_f32_e32 v208, v208
	v_exp_f32_e32 v210, v210
	v_exp_f32_e32 v212, v212
	v_exp_f32_e32 v214, v214
	v_exp_f32_e32 v216, v216
	v_exp_f32_e32 v218, v218
	v_exp_f32_e32 v220, v220
	v_med3_f32 v207, v63, s58, v195
	v_med3_f32 v209, v65, s58, v195
	v_med3_f32 v211, v59, s58, v195
	v_med3_f32 v213, v61, s58, v195
	v_med3_f32 v215, v55, s58, v195
	v_med3_f32 v217, v57, s58, v195
	v_med3_f32 v219, v51, s58, v195
	v_med3_f32 v221, v53, s58, v195
	v_pk_add_f32 v[206:207], v[206:207], v[226:227]
	v_pk_add_f32 v[208:209], v[208:209], v[226:227]
	v_pk_add_f32 v[210:211], v[210:211], v[226:227]
	v_pk_add_f32 v[212:213], v[212:213], v[226:227]
	v_pk_add_f32 v[214:215], v[214:215], v[226:227]
	v_pk_add_f32 v[216:217], v[216:217], v[226:227]
	v_pk_add_f32 v[218:219], v[218:219], v[226:227]
	v_pk_add_f32 v[220:221], v[220:221], v[226:227]
	v_rcp_f32_e32 v206, v206
	v_rcp_f32_e32 v208, v208
	v_rcp_f32_e32 v210, v210
	v_rcp_f32_e32 v212, v212
	v_rcp_f32_e32 v214, v214
	v_rcp_f32_e32 v216, v216
	v_rcp_f32_e32 v218, v218
	v_rcp_f32_e32 v220, v220
	v_mul_f32_e32 v62, v62, v206
	v_mul_f32_e32 v64, v64, v208
	v_mul_f32_e32 v58, v58, v210
	v_mul_f32_e32 v60, v60, v212
	v_mul_f32_e32 v54, v54, v214
	v_mul_f32_e32 v56, v56, v216
	v_mul_f32_e32 v50, v50, v218
	v_mul_f32_e32 v52, v52, v220
	v_mul_f32_e32 v62, v207, v62
	v_mul_f32_e32 v64, v209, v64
	v_mul_f32_e32 v58, v211, v58
	v_mul_f32_e32 v60, v213, v60
	v_mul_f32_e32 v54, v215, v54
	v_mul_f32_e32 v56, v217, v56
	v_mul_f32_e32 v50, v219, v50
	v_mul_f32_e32 v52, v221, v52
	v_cvt_pk_fp8_f32 v222, v62, v64
	v_cvt_pk_fp8_f32 v223, v54, v56
	v_add_co_u32_e32 v224, vcc, s61, v18
	s_nop 1
	v_addc_co_u32_e32 v225, vcc, 0, v19, vcc
	v_cvt_pk_fp8_f32 v222, v58, v60 op_sel:[0,0,1]
	v_cvt_pk_fp8_f32 v223, v50, v52 op_sel:[0,0,1]
	global_store_dwordx2 v[224:225], v[222:223], off
	v_min_f32_e32 v46, 0x40e00000, v46
	v_min_f32_e32 v48, 0x40e00000, v48
	v_min_f32_e32 v42, 0x40e00000, v42
	v_min_f32_e32 v44, 0x40e00000, v44
	v_min_f32_e32 v38, 0x40e00000, v38
	v_min_f32_e32 v40, 0x40e00000, v40
	v_min_f32_e32 v34, 0x40e00000, v34
	v_min_f32_e32 v36, 0x40e00000, v36
	v_mul_f32_e32 v206, 0xc01d265f, v46
	v_mul_f32_e32 v208, 0xc01d265f, v48
	v_mul_f32_e32 v210, 0xc01d265f, v42
	v_mul_f32_e32 v212, 0xc01d265f, v44
	v_mul_f32_e32 v214, 0xc01d265f, v38
	v_mul_f32_e32 v216, 0xc01d265f, v40
	v_mul_f32_e32 v218, 0xc01d265f, v34
	v_mul_f32_e32 v220, 0xc01d265f, v36
	v_exp_f32_e32 v206, v206
	v_exp_f32_e32 v208, v208
	v_exp_f32_e32 v210, v210
	v_exp_f32_e32 v212, v212
	v_exp_f32_e32 v214, v214
	v_exp_f32_e32 v216, v216
	v_exp_f32_e32 v218, v218
	v_exp_f32_e32 v220, v220
	v_med3_f32 v207, v47, s58, v195
	v_med3_f32 v209, v49, s58, v195
	v_med3_f32 v211, v43, s58, v195
	v_med3_f32 v213, v45, s58, v195
	v_med3_f32 v215, v39, s58, v195
	v_med3_f32 v217, v41, s58, v195
	v_med3_f32 v219, v35, s58, v195
	v_med3_f32 v221, v37, s58, v195
	v_pk_add_f32 v[206:207], v[206:207], v[226:227]
	v_pk_add_f32 v[208:209], v[208:209], v[226:227]
	v_pk_add_f32 v[210:211], v[210:211], v[226:227]
	v_pk_add_f32 v[212:213], v[212:213], v[226:227]
	v_pk_add_f32 v[214:215], v[214:215], v[226:227]
	v_pk_add_f32 v[216:217], v[216:217], v[226:227]
	v_pk_add_f32 v[218:219], v[218:219], v[226:227]
	v_pk_add_f32 v[220:221], v[220:221], v[226:227]
	v_rcp_f32_e32 v206, v206
	v_rcp_f32_e32 v208, v208
	v_rcp_f32_e32 v210, v210
	v_rcp_f32_e32 v212, v212
	v_rcp_f32_e32 v214, v214
	v_rcp_f32_e32 v216, v216
	v_rcp_f32_e32 v218, v218
	v_rcp_f32_e32 v220, v220
	v_mul_f32_e32 v46, v46, v206
	v_mul_f32_e32 v48, v48, v208
	v_mul_f32_e32 v42, v42, v210
	v_mul_f32_e32 v44, v44, v212
	v_mul_f32_e32 v38, v38, v214
	v_mul_f32_e32 v40, v40, v216
	v_mul_f32_e32 v34, v34, v218
	v_mul_f32_e32 v36, v36, v220
	v_mul_f32_e32 v46, v207, v46
	v_mul_f32_e32 v48, v209, v48
	v_mul_f32_e32 v42, v211, v42
	v_mul_f32_e32 v44, v213, v44
	v_mul_f32_e32 v38, v215, v38
	v_mul_f32_e32 v40, v217, v40
	v_mul_f32_e32 v34, v219, v34
	v_mul_f32_e32 v36, v221, v36
	v_cvt_pk_fp8_f32 v222, v46, v48
	v_cvt_pk_fp8_f32 v223, v38, v40
	v_add_co_u32_e32 v224, vcc, 0x58000, v18
	s_nop 1
	v_addc_co_u32_e32 v225, vcc, 0, v19, vcc
	v_cvt_pk_fp8_f32 v222, v42, v44 op_sel:[0,0,1]
	v_cvt_pk_fp8_f32 v223, v34, v36 op_sel:[0,0,1]
	global_store_dwordx2 v[224:225], v[222:223], off
	s_and_b64 vcc, exec, s[0:1]
	s_mov_b64 s[0:1], -1
	s_cbranch_vccnz .LBB0_603
	s_andn2_b64 vcc, exec, s[12:13]
	s_cbranch_vccnz .LBB0_602
	s_barrier
	s_branch .LBB0_602
